# strategy 7 (instruction selection): accumulator zeroing of the dense fp8 GEMM units uses v_mov_b64 pairs instead of 127 v_mov_b32
# baseline (speedup 1.0000x reference)
; DI void acc_zero(f32x4 (&acc)[2][2][4][2]) {
; #pragma unroll
;     for (int a = 0; a < 2; ++a)
; #pragma unroll
;         for (int b = 0; b < 2; ++b)
; #pragma unroll
;             for (int m = 0; m < 4; ++m)
; #pragma unroll
;                 for (int n = 0; n < 2; ++n) acc[a][b][m][n] = (f32x4){0.f, 0.f, 0.f, 0.f};
; }
.LBB0_175:
	s_ashr_i32 s53, s52, 31
	s_lshl_b64 s[4:5], s[52:53], 18
	s_add_u32 s54, s19, s4
	s_addc_u32 s55, s9, s5
	s_and_b64 s[4:5], s[36:37], exec
	s_cselect_b32 s53, s55, s57
	s_cselect_b32 s77, s54, s56
	s_lshl_b32 s2, s74, 18
	s_add_u32 s80, s56, 0x100
	v_mov_b32_e32 v64, 0
	v_add_u32_e32 v214, s2, v235
	v_add_u32_e32 v238, s2, v234
	v_add_u32_e32 v216, s2, v233
	v_add_u32_e32 v239, s2, v232
	v_mov_b32_e32 v217, v193
	v_mov_b32_e32 v215, v193
	s_addc_u32 s81, s57, 0
	s_mov_b32 s82, -2
	s_mov_b64 s[56:57], s[48:49]
	v_mov_b32_e32 v65, 0
	v_mov_b64_e32 v[66:67], 0
	v_mov_b64_e32 v[68:69], 0
	v_mov_b64_e32 v[70:71], 0
	v_mov_b64_e32 v[72:73], 0
	v_mov_b64_e32 v[74:75], 0
	v_mov_b64_e32 v[76:77], 0
	v_mov_b64_e32 v[78:79], 0
	v_mov_b64_e32 v[80:81], 0
	v_mov_b64_e32 v[82:83], 0
	v_mov_b64_e32 v[84:85], 0
	v_mov_b64_e32 v[86:87], 0
	v_mov_b64_e32 v[88:89], 0
	v_mov_b64_e32 v[90:91], 0
	v_mov_b64_e32 v[92:93], 0
	v_mov_b64_e32 v[94:95], 0
	v_mov_b64_e32 v[96:97], 0
	v_mov_b64_e32 v[98:99], 0
	v_mov_b64_e32 v[100:101], 0
	v_mov_b64_e32 v[102:103], 0
	v_mov_b64_e32 v[104:105], 0
	v_mov_b64_e32 v[106:107], 0
	v_mov_b64_e32 v[108:109], 0
	v_mov_b64_e32 v[110:111], 0
	v_mov_b64_e32 v[112:113], 0
	v_mov_b64_e32 v[114:115], 0
	v_mov_b64_e32 v[116:117], 0
	v_mov_b64_e32 v[118:119], 0
	v_mov_b64_e32 v[120:121], 0
	v_mov_b64_e32 v[122:123], 0
	v_mov_b64_e32 v[124:125], 0
	v_mov_b64_e32 v[126:127], 0
	v_mov_b64_e32 v[128:129], 0
	v_mov_b64_e32 v[130:131], 0
	v_mov_b64_e32 v[132:133], 0
	v_mov_b32_e32 v134, 0
	s_waitcnt vmcnt(0)
	v_mov_b32_e32 v135, 0
	v_mov_b64_e32 v[136:137], 0
	v_mov_b64_e32 v[138:139], 0
	v_mov_b64_e32 v[140:141], 0
	v_mov_b64_e32 v[142:143], 0
	v_mov_b64_e32 v[144:145], 0
	v_mov_b64_e32 v[146:147], 0
	v_mov_b64_e32 v[148:149], 0
	v_mov_b64_e32 v[150:151], 0
	v_mov_b64_e32 v[152:153], 0
	v_mov_b64_e32 v[154:155], 0
	v_mov_b64_e32 v[156:157], 0
	v_mov_b64_e32 v[158:159], 0
	v_mov_b64_e32 v[160:161], 0
	v_mov_b64_e32 v[162:163], 0
	v_mov_b64_e32 v[164:165], 0
	v_mov_b64_e32 v[166:167], 0
	v_mov_b64_e32 v[168:169], 0
	v_mov_b64_e32 v[170:171], 0
	v_mov_b64_e32 v[172:173], 0
	v_mov_b64_e32 v[174:175], 0
	v_mov_b64_e32 v[176:177], 0
	v_mov_b64_e32 v[178:179], 0
	v_mov_b64_e32 v[180:181], 0
	v_mov_b64_e32 v[182:183], 0
	v_mov_b64_e32 v[184:185], 0
	v_mov_b64_e32 v[186:187], 0
	v_mov_b64_e32 v[188:189], 0
	v_mov_b64_e32 v[190:191], 0
	s_branch .LBB0_178

; DI void acc_zero(f32x4 (&acc)[2][2][4][2]) {
; #pragma unroll
;     for (int a = 0; a < 2; ++a)
; #pragma unroll
;         for (int b = 0; b < 2; ++b)
; #pragma unroll
;             for (int m = 0; m < 4; ++m)
; #pragma unroll
;                 for (int n = 0; n < 2; ++n) acc[a][b][m][n] = (f32x4){0.f, 0.f, 0.f, 0.f};
; }
.LBB0_890:
	s_ashr_i32 s51, s50, 31
	s_lshl_b64 s[4:5], s[50:51], 18
	s_add_u32 s52, s7, s4
	s_addc_u32 s53, s8, s5
	s_and_b64 s[4:5], s[36:37], exec
	s_cselect_b32 s51, s53, s55
	s_cselect_b32 s66, s52, s54
	s_lshl_b32 s2, s63, 18
	s_add_u32 s67, s54, 0x100
	v_mov_b32_e32 v64, 0
	v_add_u32_e32 v212, s2, v233
	v_add_u32_e32 v236, s2, v232
	v_add_u32_e32 v214, s2, v231
	v_add_u32_e32 v237, s2, v230
	v_mov_b32_e32 v215, v193
	v_mov_b32_e32 v213, v193
	s_addc_u32 s68, s55, 0
	s_mov_b32 s69, -2
	s_mov_b64 s[54:55], s[46:47]
	v_mov_b32_e32 v65, 0
	v_mov_b64_e32 v[66:67], 0
	v_mov_b64_e32 v[68:69], 0
	v_mov_b64_e32 v[70:71], 0
	v_mov_b64_e32 v[72:73], 0
	v_mov_b64_e32 v[74:75], 0
	v_mov_b64_e32 v[76:77], 0
	v_mov_b64_e32 v[78:79], 0
	v_mov_b64_e32 v[80:81], 0
	v_mov_b64_e32 v[82:83], 0
	v_mov_b64_e32 v[84:85], 0
	v_mov_b64_e32 v[86:87], 0
	v_mov_b64_e32 v[88:89], 0
	v_mov_b64_e32 v[90:91], 0
	v_mov_b64_e32 v[92:93], 0
	v_mov_b64_e32 v[94:95], 0
	v_mov_b64_e32 v[96:97], 0
	v_mov_b64_e32 v[98:99], 0
	v_mov_b64_e32 v[100:101], 0
	v_mov_b64_e32 v[102:103], 0
	v_mov_b64_e32 v[104:105], 0
	v_mov_b64_e32 v[106:107], 0
	v_mov_b64_e32 v[108:109], 0
	v_mov_b64_e32 v[110:111], 0
	v_mov_b64_e32 v[112:113], 0
	v_mov_b64_e32 v[114:115], 0
	v_mov_b64_e32 v[116:117], 0
	v_mov_b64_e32 v[118:119], 0
	v_mov_b64_e32 v[120:121], 0
	v_mov_b64_e32 v[122:123], 0
	v_mov_b64_e32 v[124:125], 0
	v_mov_b64_e32 v[126:127], 0
	v_mov_b64_e32 v[128:129], 0
	v_mov_b64_e32 v[130:131], 0
	v_mov_b64_e32 v[132:133], 0
	v_mov_b32_e32 v134, 0
	s_waitcnt vmcnt(0)
	v_mov_b32_e32 v135, 0
	v_mov_b64_e32 v[136:137], 0
	v_mov_b64_e32 v[138:139], 0
	v_mov_b64_e32 v[140:141], 0
	v_mov_b64_e32 v[142:143], 0
	v_mov_b64_e32 v[144:145], 0
	v_mov_b64_e32 v[146:147], 0
	v_mov_b64_e32 v[148:149], 0
	v_mov_b64_e32 v[150:151], 0
	v_mov_b64_e32 v[152:153], 0
	v_mov_b64_e32 v[154:155], 0
	v_mov_b64_e32 v[156:157], 0
	v_mov_b64_e32 v[158:159], 0
	v_mov_b64_e32 v[160:161], 0
	v_mov_b64_e32 v[162:163], 0
	v_mov_b64_e32 v[164:165], 0
	v_mov_b64_e32 v[166:167], 0
	v_mov_b64_e32 v[168:169], 0
	v_mov_b64_e32 v[170:171], 0
	v_mov_b64_e32 v[172:173], 0
	v_mov_b64_e32 v[174:175], 0
	v_mov_b64_e32 v[176:177], 0
	v_mov_b64_e32 v[178:179], 0
	v_mov_b64_e32 v[180:181], 0
	v_mov_b64_e32 v[182:183], 0
	v_mov_b64_e32 v[184:185], 0
	v_mov_b64_e32 v[186:187], 0
	v_mov_b64_e32 v[188:189], 0
	v_mov_b64_e32 v[190:191], 0
	s_branch .LBB0_893
